# v67 + remaining cross-row shuffles (PLE epilogue sum-of-squares x16, ret_out group norm x4) via v_permlane16/32_swap instead of ds_bpermute
# baseline (speedup 1.0000x reference)
; DI void ret_out_unit(const Ctx& c, int u) {
;     ...
;     float s = 0.f;
; #pragma unroll
;     for (int ef = 0; ef < 8; ++ef) s += (acc[ef][0] + acc[ef][1]) + (acc[ef][2] + acc[ef][3]);
;     s += __shfl_xor(s, 16); s += __shfl_xor(s, 32);
;     const float mean = s * (1.0f / 128.0f); float qv = 0.f;
; #pragma unroll
;     for (int ef = 0; ef < 8; ++ef) { const f32x4 dlt = acc[ef] - mean; qv += (dlt[0] * dlt[0] + dlt[1] * dlt[1]) + (dlt[2] * dlt[2] + dlt[3] * dlt[3]); }
;     qv += __shfl_xor(qv, 16); qv += __shfl_xor(qv, 32);
;     const float rstd = rsqrtf(qv * (1.0f / 128.0f) + LN_EPS);
.LBB0_272:
	s_nop 4
	v_mov_b32_e32 v64, v56
	v_mov_b32_e32 v65, v60
	v_mov_b32_e32 v66, v57
	v_mov_b32_e32 v67, v61
	v_pk_add_f32 v[64:65], v[64:65], v[66:67]
	v_mov_b32_e32 v66, v58
	v_mov_b32_e32 v67, v62
	v_mov_b32_e32 v68, v59
	v_mov_b32_e32 v69, v63
	v_pk_add_f32 v[66:67], v[66:67], v[68:69]
	v_mov_b32_e32 v68, v52
	v_pk_add_f32 v[64:65], v[64:65], v[66:67]
	v_mov_b32_e32 v66, v53
	v_mov_b32_e32 v67, v54
	v_mov_b32_e32 v69, v55
	v_pk_add_f32 v[66:67], v[66:67], v[68:69]
	v_add_f32_e32 v65, 0, v65
	v_pk_add_f32 v[66:67], v[66:67], v[66:67] op_sel_hi:[0,1]
	v_add_f32_e32 v65, v64, v65
	v_add_f32_e32 v69, v48, v49
	v_add_f32_e32 v71, v50, v51
	v_mov_b32_e32 v68, v44
	v_mov_b32_e32 v70, v45
	v_mov_b32_e32 v66, v46
	v_mov_b32_e32 v64, v47
	v_pk_add_f32 v[68:69], v[68:69], v[70:71]
	v_pk_add_f32 v[64:65], v[66:67], v[64:65]
	v_mov_b32_e32 v66, v41
	v_pk_add_f32 v[64:65], v[68:69], v[64:65]
	v_mov_b32_e32 v67, v42
	v_mov_b32_e32 v68, v40
	v_mov_b32_e32 v69, v43
	v_pk_add_f32 v[66:67], v[66:67], v[68:69]
	v_pk_add_f32 v[64:65], v[64:65], v[64:65] op_sel_hi:[0,1]
	v_pk_add_f32 v[66:67], v[66:67], v[66:67] op_sel_hi:[0,1]
	v_add_f32_e32 v69, v36, v37
	v_add_f32_e32 v71, v38, v39
	v_mov_b32_e32 v68, v32
	v_mov_b32_e32 v70, v33
	v_mov_b32_e32 v66, v34
	v_mov_b32_e32 v64, v35
	v_pk_add_f32 v[68:69], v[68:69], v[70:71]
	v_pk_add_f32 v[64:65], v[66:67], v[64:65]
	v_and_b32_e32 v66, 64, v123
	v_pk_add_f32 v[64:65], v[68:69], v[64:65]
	v_add_u32_e32 v66, 64, v66
	v_add_f32_e32 v64, v64, v65
	v_xor_b32_e32 v65, 16, v123
	v_cmp_lt_i32_e32 vcc, v65, v66
	s_lshl_b32 s30, s6, 1
	v_ashrrev_i32_e32 v105, 31, v104
	v_cndmask_b32_e32 v65, v123, v65, vcc
	v_lshlrev_b32_e32 v72, 2, v65
	v_mov_b32_e32 v65, v64
	s_nop 1
	v_permlane16_swap_b32 v64, v65
	s_add_i32 s85, s85, s44
	s_add_i32 s84, s84, 1
	s_cmpk_gt_i32 s85, 0x1ff
	s_waitcnt lgkmcnt(0)
	v_add_f32_e32 v64, v64, v65
	v_xor_b32_e32 v65, 32, v123
	v_cmp_lt_i32_e32 vcc, v65, v66
	s_nop 1
	v_cndmask_b32_e32 v65, v123, v65, vcc
	v_lshlrev_b32_e32 v73, 2, v65
	v_mov_b32_e32 v65, v64
	s_nop 1
	v_permlane32_swap_b32 v64, v65
	s_waitcnt lgkmcnt(0)
	v_add_f32_e32 v74, v64, v65
	v_fmamk_f32 v64, v74, 0xbc000000, v63
	v_fmamk_f32 v68, v74, 0xbc000000, v61
	v_fmamk_f32 v65, v74, 0xbc000000, v59
	v_fmamk_f32 v69, v74, 0xbc000000, v57
	v_fmamk_f32 v66, v74, 0xbc000000, v62
	v_fmamk_f32 v70, v74, 0xbc000000, v60
	v_fmamk_f32 v67, v74, 0xbc000000, v58
	v_fmamk_f32 v71, v74, 0xbc000000, v56
	v_pk_mul_f32 v[68:69], v[68:69], v[68:69]
	v_pk_mul_f32 v[64:65], v[64:65], v[64:65]
	v_pk_fma_f32 v[68:69], v[70:71], v[70:71], v[68:69]
	v_pk_fma_f32 v[64:65], v[66:67], v[66:67], v[64:65]
	v_fmamk_f32 v67, v74, 0xbc000000, v53
	v_pk_add_f32 v[64:65], v[68:69], v[64:65]
	v_fmamk_f32 v66, v74, 0xbc000000, v52
	v_fmamk_f32 v69, v74, 0xbc000000, v55
	v_fmamk_f32 v68, v74, 0xbc000000, v54
	v_pk_mul_f32 v[68:69], v[68:69], v[68:69]
	v_pk_mul_f32 v[66:67], v[66:67], v[66:67]
	v_pk_add_f32 v[64:65], v[64:65], v[64:65] op_sel_hi:[0,1]
	v_pk_mov_b32 v[70:71], v[66:67], v[68:69] op_sel:[1,0]
	v_mov_b32_e32 v67, v69
	v_fmamk_f32 v68, v74, 0xbc000000, v48
	v_pk_add_f32 v[66:67], v[70:71], v[66:67]
	v_fmamk_f32 v69, v74, 0xbc000000, v49
	v_fmamk_f32 v70, v74, 0xbc000000, v50
	v_mul_f32_e32 v64, v68, v68
	v_fmamk_f32 v71, v74, 0xbc000000, v51
	v_pk_fma_f32 v[68:69], v[68:69], v[68:69], v[64:65] op_sel_hi:[1,1,0]
	v_mul_f32_e32 v64, v70, v70
	v_pk_add_f32 v[66:67], v[66:67], v[66:67] op_sel_hi:[0,1]
	v_pk_fma_f32 v[70:71], v[70:71], v[70:71], v[64:65] op_sel_hi:[1,1,0]
	v_fmamk_f32 v64, v74, 0xbc000000, v47
	v_fmamk_f32 v66, v74, 0xbc000000, v46
	v_fmamk_f32 v70, v74, 0xbc000000, v45
	v_fmamk_f32 v68, v74, 0xbc000000, v44
	v_mul_f32_e32 v68, v68, v68
	v_mul_f32_e32 v70, v70, v70
	v_mul_f32_e32 v66, v66, v66
	v_mul_f32_e32 v64, v64, v64
	v_pk_add_f32 v[68:69], v[68:69], v[70:71]
	v_pk_add_f32 v[64:65], v[66:67], v[64:65]
	v_fmamk_f32 v67, v74, 0xbc000000, v41
	v_pk_add_f32 v[64:65], v[68:69], v[64:65]
	v_fmamk_f32 v66, v74, 0xbc000000, v40
	v_fmamk_f32 v69, v74, 0xbc000000, v43
	v_fmamk_f32 v68, v74, 0xbc000000, v42
	v_pk_mul_f32 v[68:69], v[68:69], v[68:69]
	v_pk_mul_f32 v[66:67], v[66:67], v[66:67]
	v_pk_add_f32 v[64:65], v[64:65], v[64:65] op_sel_hi:[0,1]
	v_pk_mov_b32 v[70:71], v[66:67], v[68:69] op_sel:[1,0]
	v_mov_b32_e32 v67, v69
	v_fmamk_f32 v68, v74, 0xbc000000, v36
	v_pk_add_f32 v[66:67], v[70:71], v[66:67]
	v_fmamk_f32 v69, v74, 0xbc000000, v37
	v_fmamk_f32 v70, v74, 0xbc000000, v38
	v_mul_f32_e32 v64, v68, v68
	v_fmamk_f32 v71, v74, 0xbc000000, v39
	v_pk_fma_f32 v[68:69], v[68:69], v[68:69], v[64:65] op_sel_hi:[1,1,0]
	v_mul_f32_e32 v64, v70, v70
	v_pk_add_f32 v[66:67], v[66:67], v[66:67] op_sel_hi:[0,1]
	v_pk_fma_f32 v[70:71], v[70:71], v[70:71], v[64:65] op_sel_hi:[1,1,0]
	v_fmamk_f32 v64, v74, 0xbc000000, v35
	v_fmamk_f32 v66, v74, 0xbc000000, v34
	v_fmamk_f32 v70, v74, 0xbc000000, v33
	v_fmamk_f32 v68, v74, 0xbc000000, v32
	v_mul_f32_e32 v68, v68, v68
	v_mul_f32_e32 v70, v70, v70
	v_mul_f32_e32 v66, v66, v66
	v_mul_f32_e32 v64, v64, v64
	v_pk_add_f32 v[68:69], v[68:69], v[70:71]
	v_pk_add_f32 v[64:65], v[66:67], v[64:65]
	v_lshlrev_b32_e32 v70, 16, v102
	v_pk_add_f32 v[64:65], v[68:69], v[64:65]
	v_and_b32_e32 v71, 0xffff0000, v102
	v_add_f32_e32 v64, v64, v65
	v_mov_b32_e32 v65, v64
	s_nop 1
	v_permlane16_swap_b32 v64, v65
	v_mul_f32_e32 v67, 0xbfb8aa3b, v71
	v_exp_f32_e32 v67, v67
	v_add_u32_e32 v68, s86, v86
	v_ashrrev_i32_e32 v69, 31, v68
	s_waitcnt lgkmcnt(0)
	v_add_f32_e32 v64, v64, v65
	v_mov_b32_e32 v65, v64
	s_nop 1
	v_permlane32_swap_b32 v64, v65
	v_lshlrev_b64 v[68:69], 12, v[68:69]
	v_lshl_add_u64 v[68:69], s[28:29], 0, v[68:69]
	v_lshl_add_u64 v[68:69], v[68:69], 0, s[30:31]
	s_waitcnt lgkmcnt(0)
; DI float bflo(unsigned w) { return __uint_as_float(w << 16); }
; DI float bfhi(unsigned w) { return __uint_as_float(w & 0xffff0000u); }
; DI u32x2 pack4(f32x4 v) { bf16x4_t r = __builtin_convertvector(v, bf16x4_t); return __builtin_bit_cast(u32x2, r); }
; DI float sigmoidf_(float x) { return __builtin_amdgcn_rcpf(1.0f + __expf(-x)); }
; DI void ret_out_unit(const Ctx& c, int u) {
;     ...
;     const float rstd = rsqrtf(qv * (1.0f / 128.0f) + LN_EPS);
;     u16* mixed = (u16*)(c.ws + WS_MIXED);
;     const size_t trow = (size_t)(t0 + il);
; #pragma unroll
;     for (int ef = 0; ef < 8; ++ef) { const int e = ef * 16 + 4 * fq; const f32x4 gw = gwv[ef];
;         const u32x2 gb = gbv[ef];
;         const float g[4] = {bflo(gb.x), bfhi(gb.x), bflo(gb.y), bfhi(gb.y)}; f32x4 o;
; #pragma unroll
;         for (int r = 0; r < 4; ++r) o[r] = (acc[ef][r] - mean) * rstd * gw[r] * (g[r] * sigmoidf_(g[r]));
;         *(u32x2*)(mixed + trow * D + h * 128 + e) = pack4(o); }
	v_add_f32_e32 v64, v64, v65
	v_fmamk_f32 v64, v64, 0x3c000000, v120
	v_mul_f32_e32 v65, 0x4b800000, v64
	v_cmp_gt_f32_e32 vcc, s83, v64
	s_nop 1
	v_cndmask_b32_e32 v64, v64, v65, vcc
	v_rsq_f32_e32 v65, v64
	v_mul_f32_e32 v64, 0x3c000000, v74
	v_mul_f32_e32 v66, 0x45800000, v65
	v_cndmask_b32_e32 v66, v65, v66, vcc
	v_mul_f32_e32 v65, 0xbfb8aa3b, v70
	v_exp_f32_e32 v65, v65
	s_nop 0
	v_add_f32_e32 v65, 1.0, v65
	v_rcp_f32_e32 v72, v65
	v_add_f32_e32 v65, 1.0, v67
	v_rcp_f32_e32 v73, v65
	v_pk_add_f32 v[60:61], v[60:61], v[64:65] op_sel_hi:[1,0] neg_lo:[0,1] neg_hi:[0,1]
	s_nop 0
	v_pk_mul_f32 v[60:61], v[60:61], v[66:67] op_sel_hi:[1,0]
	s_nop 0
	v_pk_mul_f32 v[28:29], v[28:29], v[60:61]
	v_pk_mul_f32 v[60:61], v[72:73], v[70:71]
	v_lshlrev_b32_e32 v70, 16, v103
	v_and_b32_e32 v71, 0xffff0000, v103
	v_mul_f32_e32 v65, 0xbfb8aa3b, v70
	v_mul_f32_e32 v67, 0xbfb8aa3b, v71
	v_exp_f32_e32 v65, v65
	v_exp_f32_e32 v67, v67
	v_pk_mul_f32 v[28:29], v[60:61], v[28:29]
	v_add_f32_e32 v60, 1.0, v65
	v_add_f32_e32 v61, 1.0, v67
	v_rcp_f32_e32 v60, v60
	v_rcp_f32_e32 v61, v61
	v_pk_add_f32 v[62:63], v[62:63], v[64:65] op_sel_hi:[1,0] neg_lo:[0,1] neg_hi:[0,1]
	v_pk_add_f32 v[56:57], v[56:57], v[64:65] op_sel_hi:[1,0] neg_lo:[0,1] neg_hi:[0,1]
	v_pk_mul_f32 v[62:63], v[62:63], v[66:67] op_sel_hi:[1,0]
	v_pk_mul_f32 v[60:61], v[60:61], v[70:71]
	v_pk_mul_f32 v[30:31], v[30:31], v[62:63]
	v_pk_mul_f32 v[56:57], v[56:57], v[66:67] op_sel_hi:[1,0]
	v_pk_mul_f32 v[30:31], v[60:61], v[30:31]
	v_lshlrev_b32_e32 v60, 16, v100
	v_and_b32_e32 v61, 0xffff0000, v100
	v_mul_f32_e32 v62, 0xbfb8aa3b, v60
	v_mul_f32_e32 v63, 0xbfb8aa3b, v61
	v_exp_f32_e32 v62, v62
	v_exp_f32_e32 v63, v63
	v_cvt_pk_bf16_f32 v31, v30, v31
	v_cvt_pk_bf16_f32 v30, v28, v29
	v_lshl_add_u64 v[28:29], v[104:105], 1, v[68:69]
	global_store_dwordx2 v[28:29], v[30:31], off
	v_add_f32_e32 v30, 1.0, v62
	v_add_f32_e32 v31, 1.0, v63
	v_rcp_f32_e32 v30, v30
	v_rcp_f32_e32 v31, v31
	v_pk_mul_f32 v[24:25], v[24:25], v[56:57]
	v_lshlrev_b32_e32 v56, 16, v101
	v_and_b32_e32 v57, 0xffff0000, v101
	v_pk_mul_f32 v[30:31], v[30:31], v[60:61]
	v_mul_f32_e32 v60, 0xbfb8aa3b, v56
	v_mul_f32_e32 v61, 0xbfb8aa3b, v57
	v_exp_f32_e32 v60, v60
	v_exp_f32_e32 v61, v61
	v_pk_mul_f32 v[24:25], v[30:31], v[24:25]
	v_pk_add_f32 v[58:59], v[58:59], v[64:65] op_sel_hi:[1,0] neg_lo:[0,1] neg_hi:[0,1]
	v_add_f32_e32 v30, 1.0, v60
	v_add_f32_e32 v31, 1.0, v61
	v_rcp_f32_e32 v30, v30
	v_rcp_f32_e32 v31, v31
	v_pk_mul_f32 v[58:59], v[58:59], v[66:67] op_sel_hi:[1,0]
	v_pk_mul_f32 v[30:31], v[30:31], v[56:57]
	v_pk_mul_f32 v[26:27], v[26:27], v[58:59]
	s_nop 0
	v_pk_mul_f32 v[26:27], v[30:31], v[26:27]
	s_nop 0
	v_cvt_pk_bf16_f32 v27, v26, v27
	v_cvt_pk_bf16_f32 v26, v24, v25
	v_lshlrev_b32_e32 v24, 16, v98
	v_and_b32_e32 v25, 0xffff0000, v98
	v_mul_f32_e32 v30, 0xbfb8aa3b, v24
	v_mul_f32_e32 v31, 0xbfb8aa3b, v25
	v_exp_f32_e32 v30, v30
	v_exp_f32_e32 v31, v31
	global_store_dwordx2 v[28:29], v[26:27], off offset:32
	v_add_f32_e32 v26, 1.0, v30
	v_add_f32_e32 v27, 1.0, v31
	v_rcp_f32_e32 v26, v26
	v_rcp_f32_e32 v27, v27
	v_pk_add_f32 v[30:31], v[52:53], v[64:65] op_sel_hi:[1,0] neg_lo:[0,1] neg_hi:[0,1]
	v_pk_mul_f32 v[24:25], v[26:27], v[24:25]
	v_pk_mul_f32 v[30:31], v[30:31], v[66:67] op_sel_hi:[1,0]
	v_lshlrev_b32_e32 v26, 16, v99
	v_and_b32_e32 v27, 0xffff0000, v99
	v_pk_mul_f32 v[20:21], v[20:21], v[30:31]
	v_mul_f32_e32 v30, 0xbfb8aa3b, v26
	v_mul_f32_e32 v31, 0xbfb8aa3b, v27
	v_exp_f32_e32 v30, v30
	v_exp_f32_e32 v31, v31
	v_pk_mul_f32 v[20:21], v[24:25], v[20:21]
	v_add_f32_e32 v24, 1.0, v30
	v_add_f32_e32 v25, 1.0, v31
	v_rcp_f32_e32 v24, v24
	v_rcp_f32_e32 v25, v25
	v_pk_add_f32 v[30:31], v[54:55], v[64:65] op_sel_hi:[1,0] neg_lo:[0,1] neg_hi:[0,1]
	v_pk_mul_f32 v[24:25], v[24:25], v[26:27]
	v_pk_mul_f32 v[30:31], v[30:31], v[66:67] op_sel_hi:[1,0]
	s_nop 0
	v_pk_mul_f32 v[22:23], v[22:23], v[30:31]
	s_nop 0
	v_pk_mul_f32 v[22:23], v[24:25], v[22:23]
	s_nop 0
	v_cvt_pk_bf16_f32 v23, v22, v23
	v_cvt_pk_bf16_f32 v22, v20, v21
	v_lshlrev_b32_e32 v20, 16, v96
	v_and_b32_e32 v21, 0xffff0000, v96
	v_mul_f32_e32 v24, 0xbfb8aa3b, v20
	v_mul_f32_e32 v25, 0xbfb8aa3b, v21
	v_exp_f32_e32 v24, v24
	v_exp_f32_e32 v25, v25
	global_store_dwordx2 v[28:29], v[22:23], off offset:64
	v_add_f32_e32 v22, 1.0, v24
	v_add_f32_e32 v23, 1.0, v25
	v_rcp_f32_e32 v22, v22
	v_rcp_f32_e32 v23, v23
	v_pk_add_f32 v[24:25], v[48:49], v[64:65] op_sel_hi:[1,0] neg_lo:[0,1] neg_hi:[0,1]
	v_pk_mul_f32 v[20:21], v[22:23], v[20:21]
	v_pk_mul_f32 v[24:25], v[24:25], v[66:67] op_sel_hi:[1,0]
	v_lshlrev_b32_e32 v22, 16, v97
	v_and_b32_e32 v23, 0xffff0000, v97
	v_pk_mul_f32 v[16:17], v[16:17], v[24:25]
	v_mul_f32_e32 v24, 0xbfb8aa3b, v22
	v_mul_f32_e32 v25, 0xbfb8aa3b, v23
	v_exp_f32_e32 v24, v24
	v_exp_f32_e32 v25, v25
	v_pk_mul_f32 v[16:17], v[20:21], v[16:17]
	v_add_f32_e32 v20, 1.0, v24
	v_add_f32_e32 v21, 1.0, v25
	v_rcp_f32_e32 v20, v20
	v_rcp_f32_e32 v21, v21
	v_pk_add_f32 v[24:25], v[50:51], v[64:65] op_sel_hi:[1,0] neg_lo:[0,1] neg_hi:[0,1]
	v_pk_mul_f32 v[20:21], v[20:21], v[22:23]
	v_pk_mul_f32 v[24:25], v[24:25], v[66:67] op_sel_hi:[1,0]
	s_nop 0
	v_pk_mul_f32 v[18:19], v[18:19], v[24:25]
	s_nop 0
; DI float bflo(unsigned w) { return __uint_as_float(w << 16); }
; DI float bfhi(unsigned w) { return __uint_as_float(w & 0xffff0000u); }
; DI u32x2 pack4(f32x4 v) { bf16x4_t r = __builtin_convertvector(v, bf16x4_t); return __builtin_bit_cast(u32x2, r); }
; DI float sigmoidf_(float x) { return __builtin_amdgcn_rcpf(1.0f + __expf(-x)); }
; DI void ret_out_unit(const Ctx& c, int u) {
;     ...
;     for (int ef = 0; ef < 8; ++ef) { const int e = ef * 16 + 4 * fq; const f32x4 gw = gwv[ef];
;         const u32x2 gb = gbv[ef];
;         const float g[4] = {bflo(gb.x), bfhi(gb.x), bflo(gb.y), bfhi(gb.y)}; f32x4 o;
; #pragma unroll
;         for (int r = 0; r < 4; ++r) o[r] = (acc[ef][r] - mean) * rstd * gw[r] * (g[r] * sigmoidf_(g[r]));
;         *(u32x2*)(mixed + trow * D + h * 128 + e) = pack4(o); }
	v_pk_mul_f32 v[18:19], v[20:21], v[18:19]
	s_nop 0
	v_cvt_pk_bf16_f32 v19, v18, v19
	v_cvt_pk_bf16_f32 v18, v16, v17
	v_lshlrev_b32_e32 v16, 16, v94
	v_and_b32_e32 v17, 0xffff0000, v94
	v_mul_f32_e32 v20, 0xbfb8aa3b, v16
	v_mul_f32_e32 v21, 0xbfb8aa3b, v17
	v_exp_f32_e32 v20, v20
	v_exp_f32_e32 v21, v21
	global_store_dwordx2 v[28:29], v[18:19], off offset:96
	v_add_f32_e32 v18, 1.0, v20
	v_add_f32_e32 v19, 1.0, v21
	v_rcp_f32_e32 v18, v18
	v_rcp_f32_e32 v19, v19
	v_pk_add_f32 v[20:21], v[44:45], v[64:65] op_sel_hi:[1,0] neg_lo:[0,1] neg_hi:[0,1]
	v_pk_mul_f32 v[16:17], v[18:19], v[16:17]
	v_pk_mul_f32 v[20:21], v[20:21], v[66:67] op_sel_hi:[1,0]
	v_lshlrev_b32_e32 v18, 16, v95
	v_and_b32_e32 v19, 0xffff0000, v95
	v_pk_mul_f32 v[12:13], v[12:13], v[20:21]
	v_mul_f32_e32 v20, 0xbfb8aa3b, v18
	v_mul_f32_e32 v21, 0xbfb8aa3b, v19
	v_exp_f32_e32 v20, v20
	v_exp_f32_e32 v21, v21
	v_pk_mul_f32 v[12:13], v[16:17], v[12:13]
	v_add_f32_e32 v16, 1.0, v20
	v_add_f32_e32 v17, 1.0, v21
	v_rcp_f32_e32 v16, v16
	v_rcp_f32_e32 v17, v17
	v_pk_add_f32 v[20:21], v[46:47], v[64:65] op_sel_hi:[1,0] neg_lo:[0,1] neg_hi:[0,1]
	v_pk_mul_f32 v[16:17], v[16:17], v[18:19]
	v_pk_mul_f32 v[20:21], v[20:21], v[66:67] op_sel_hi:[1,0]
	s_nop 0
	v_pk_mul_f32 v[14:15], v[14:15], v[20:21]
	s_nop 0
	v_pk_mul_f32 v[14:15], v[16:17], v[14:15]
	s_nop 0
	v_cvt_pk_bf16_f32 v15, v14, v15
	v_cvt_pk_bf16_f32 v14, v12, v13
	v_lshlrev_b32_e32 v12, 16, v92
	v_and_b32_e32 v13, 0xffff0000, v92
	v_mul_f32_e32 v16, 0xbfb8aa3b, v12
	v_mul_f32_e32 v17, 0xbfb8aa3b, v13
	v_exp_f32_e32 v16, v16
	v_exp_f32_e32 v17, v17
	global_store_dwordx2 v[28:29], v[14:15], off offset:128
	v_add_f32_e32 v14, 1.0, v16
	v_add_f32_e32 v15, 1.0, v17
	v_rcp_f32_e32 v14, v14
	v_rcp_f32_e32 v15, v15
	v_pk_add_f32 v[16:17], v[40:41], v[64:65] op_sel_hi:[1,0] neg_lo:[0,1] neg_hi:[0,1]
	v_pk_mul_f32 v[12:13], v[14:15], v[12:13]
	v_pk_mul_f32 v[16:17], v[16:17], v[66:67] op_sel_hi:[1,0]
	v_lshlrev_b32_e32 v14, 16, v93
	v_and_b32_e32 v15, 0xffff0000, v93
	v_pk_mul_f32 v[8:9], v[8:9], v[16:17]
	v_mul_f32_e32 v16, 0xbfb8aa3b, v14
	v_mul_f32_e32 v17, 0xbfb8aa3b, v15
	v_exp_f32_e32 v16, v16
	v_exp_f32_e32 v17, v17
	v_pk_mul_f32 v[8:9], v[12:13], v[8:9]
	v_add_f32_e32 v12, 1.0, v16
	v_add_f32_e32 v13, 1.0, v17
	v_rcp_f32_e32 v12, v12
	v_rcp_f32_e32 v13, v13
	v_pk_add_f32 v[16:17], v[42:43], v[64:65] op_sel_hi:[1,0] neg_lo:[0,1] neg_hi:[0,1]
	v_pk_mul_f32 v[12:13], v[12:13], v[14:15]
	v_pk_mul_f32 v[16:17], v[16:17], v[66:67] op_sel_hi:[1,0]
	s_nop 0
	v_pk_mul_f32 v[10:11], v[10:11], v[16:17]
	s_nop 0
	v_pk_mul_f32 v[10:11], v[12:13], v[10:11]
	s_nop 0
	v_cvt_pk_bf16_f32 v11, v10, v11
	v_cvt_pk_bf16_f32 v10, v8, v9
	v_lshlrev_b32_e32 v8, 16, v90
	v_and_b32_e32 v9, 0xffff0000, v90
	v_mul_f32_e32 v12, 0xbfb8aa3b, v8
	v_mul_f32_e32 v13, 0xbfb8aa3b, v9
	v_exp_f32_e32 v12, v12
	v_exp_f32_e32 v13, v13
	global_store_dwordx2 v[28:29], v[10:11], off offset:160
	v_add_f32_e32 v10, 1.0, v12
	v_add_f32_e32 v11, 1.0, v13
	v_rcp_f32_e32 v10, v10
	v_rcp_f32_e32 v11, v11
	v_pk_add_f32 v[12:13], v[36:37], v[64:65] op_sel_hi:[1,0] neg_lo:[0,1] neg_hi:[0,1]
	v_pk_mul_f32 v[8:9], v[10:11], v[8:9]
	v_pk_mul_f32 v[12:13], v[12:13], v[66:67] op_sel_hi:[1,0]
	v_lshlrev_b32_e32 v10, 16, v91
	v_and_b32_e32 v11, 0xffff0000, v91
	v_pk_mul_f32 v[4:5], v[4:5], v[12:13]
	v_mul_f32_e32 v12, 0xbfb8aa3b, v10
	v_mul_f32_e32 v13, 0xbfb8aa3b, v11
	v_exp_f32_e32 v12, v12
	v_exp_f32_e32 v13, v13
	v_pk_mul_f32 v[4:5], v[8:9], v[4:5]
	v_add_f32_e32 v8, 1.0, v12
	v_add_f32_e32 v9, 1.0, v13
	v_rcp_f32_e32 v8, v8
	v_rcp_f32_e32 v9, v9
	v_pk_add_f32 v[12:13], v[38:39], v[64:65] op_sel_hi:[1,0] neg_lo:[0,1] neg_hi:[0,1]
	v_pk_mul_f32 v[8:9], v[8:9], v[10:11]
	v_pk_mul_f32 v[12:13], v[12:13], v[66:67] op_sel_hi:[1,0]
	s_nop 0
	v_pk_mul_f32 v[6:7], v[6:7], v[12:13]
	s_nop 0
	v_pk_mul_f32 v[6:7], v[8:9], v[6:7]
	s_nop 0
	v_cvt_pk_bf16_f32 v7, v6, v7
	v_cvt_pk_bf16_f32 v6, v4, v5
	v_lshlrev_b32_e32 v4, 16, v88
	v_and_b32_e32 v5, 0xffff0000, v88
	v_mul_f32_e32 v8, 0xbfb8aa3b, v4
	v_mul_f32_e32 v9, 0xbfb8aa3b, v5
	v_exp_f32_e32 v8, v8
	v_exp_f32_e32 v9, v9
	global_store_dwordx2 v[28:29], v[6:7], off offset:192
	v_add_f32_e32 v6, 1.0, v8
	v_add_f32_e32 v7, 1.0, v9
	v_rcp_f32_e32 v6, v6
	v_rcp_f32_e32 v7, v7
	v_pk_add_f32 v[8:9], v[32:33], v[64:65] op_sel_hi:[1,0] neg_lo:[0,1] neg_hi:[0,1]
	v_pk_mul_f32 v[4:5], v[6:7], v[4:5]
	v_pk_mul_f32 v[8:9], v[8:9], v[66:67] op_sel_hi:[1,0]
	v_lshlrev_b32_e32 v6, 16, v89
	v_and_b32_e32 v7, 0xffff0000, v89
	v_pk_mul_f32 v[0:1], v[0:1], v[8:9]
	v_mul_f32_e32 v8, 0xbfb8aa3b, v6
	v_mul_f32_e32 v9, 0xbfb8aa3b, v7
	v_exp_f32_e32 v8, v8
	v_exp_f32_e32 v9, v9
	v_pk_mul_f32 v[0:1], v[4:5], v[0:1]
	v_add_f32_e32 v4, 1.0, v8
	v_add_f32_e32 v5, 1.0, v9
	v_rcp_f32_e32 v4, v4
	v_rcp_f32_e32 v5, v5
	v_pk_add_f32 v[8:9], v[34:35], v[64:65] op_sel_hi:[1,0] neg_lo:[0,1] neg_hi:[0,1]
	v_pk_mul_f32 v[4:5], v[4:5], v[6:7]
	v_pk_mul_f32 v[8:9], v[8:9], v[66:67] op_sel_hi:[1,0]
	s_nop 0
	v_pk_mul_f32 v[2:3], v[2:3], v[8:9]
	s_nop 0
	v_pk_mul_f32 v[2:3], v[4:5], v[2:3]
	s_nop 0
	v_cvt_pk_bf16_f32 v3, v2, v3
	v_cvt_pk_bf16_f32 v2, v0, v1
	global_store_dwordx2 v[28:29], v[2:3], off offset:224
	s_cbranch_scc1 .LBB0_312

; #define G_SETUP_B(u) do { rsB0 = mk_rsrc((u).b0); rsB1 = mk_rsrc((u).b1); } while (0)
;     ...
;         U nxt = cur;
;         const bool has_next = sched.get(ui + 1, nxt);
;         G_SETUP_B(nxt);
;         G_TILE(G_A0, G_B0, true, G_B1, G_A1, nt - 1, true, 0, G_SETUP_A(nxt));
.LBB0_903:
	s_mov_b32 m0, s64
	ds_read_b64_tr_b16 v[170:171], v166
	ds_read_b64_tr_b16 v[174:175], v166 offset:32
	ds_read_b64_tr_b16 v[178:179], v166 offset:64
	ds_read_b64_tr_b16 v[182:183], v166 offset:96
	ds_read_b64_tr_b16 v[172:173], v167
	ds_read_b64_tr_b16 v[176:177], v167 offset:32
	ds_read_b64_tr_b16 v[180:181], v167 offset:64
	ds_read_b64_tr_b16 v[184:185], v167 offset:96
	ds_read_b128 v[186:189], v162
	ds_read_b128 v[190:193], v162 offset:2048
	ds_read_b128 v[198:201], v162 offset:4096
	buffer_load_dwordx4 v163, s[20:23], s65 offen lds
	s_mov_b32 m0, s63
	s_waitcnt lgkmcnt(2)
	v_mfma_f32_16x16x32_bf16 v[152:155], v[174:177], v[186:189], v[152:155]
	buffer_load_dwordx4 v165, s[20:23], s65 offen lds
	s_mov_b32 m0, s62
	s_and_b32 s13, s48, 0xffff
	buffer_load_dwordx4 v164, s[20:23], s65 offen lds
	s_mov_b32 m0, s31
	v_mfma_f32_16x16x32_bf16 v[148:151], v[178:181], v[186:189], v[148:151]
	buffer_load_dwordx4 v168, s[20:23], s65 offen lds
	v_mbcnt_lo_u32_b32 v163, -1, 0
	v_mbcnt_hi_u32_b32 v163, -1, v163
	s_and_b32 s17, s51, 0xffff
	v_lshlrev_b32_e32 v164, 4, v163
	v_and_b32_e32 v165, 32, v163
	v_lshrrev_b32_e32 v163, 2, v163
	v_mfma_f32_16x16x32_bf16 v[144:147], v[182:185], v[186:189], v[144:147]
	v_bitop3_b32 v164, v164, v165, 48 bitop3:0x6c
	v_add_lshl_u32 v163, v163, s52, 9
	v_or3_b32 v163, v164, s53, v163
	s_mov_b32 s18, s14
	s_mov_b32 s19, s15
	s_and_b32 s21, s46, 0xffff
	s_mov_b32 s22, s14
	s_mov_b32 s23, s15
	v_add_u32_e32 v165, 0x8000, v163
	v_add_u32_e32 v164, 0x10000, v163
	v_add_u32_e32 v168, 0x18000, v163
	s_mov_b32 s12, s47
	s_mov_b32 s16, s50
	s_mov_b32 s20, s7
	v_mfma_f32_16x16x32_bf16 v[156:159], v[170:173], v[186:189], v[156:159]
	s_waitcnt vmcnt(11)
	v_cvt_pk_bf16_f32 v15, v14, v15
	v_cvt_pk_bf16_f32 v14, v12, v13
	s_waitcnt lgkmcnt(1)
	v_mfma_f32_16x16x32_bf16 v[140:143], v[170:173], v[190:193], v[140:143]
	ds_read_b128 v[186:189], v162 offset:6144
	ds_write_b64 v161, v[14:15] offset:34816
	v_mfma_f32_16x16x32_bf16 v[136:139], v[174:177], v[190:193], v[136:139]
	v_mfma_f32_16x16x32_bf16 v[132:135], v[178:181], v[190:193], v[132:135]
	v_mfma_f32_16x16x32_bf16 v[12:15], v[182:185], v[190:193], v[128:131]
	s_nop 2
	buffer_load_dwordx4 v[128:131], v160, s[12:15], 0 offen
	s_waitcnt lgkmcnt(2)
	v_mfma_f32_16x16x32_bf16 v[124:127], v[170:173], v[198:201], v[124:127]
	ds_read_b128 v[190:193], v162 offset:8192
	v_mfma_f32_16x16x32_bf16 v[120:123], v[174:177], v[198:201], v[120:123]
	v_mfma_f32_16x16x32_bf16 v[116:119], v[178:181], v[198:201], v[116:119]
	v_mfma_f32_16x16x32_bf16 v[112:115], v[182:185], v[198:201], v[112:115]
	s_waitcnt vmcnt(11)
	v_cvt_pk_bf16_f32 v3, v2, v3
	v_cvt_pk_bf16_f32 v2, v0, v1
	s_waitcnt lgkmcnt(2)
	v_mfma_f32_16x16x32_bf16 v[108:111], v[170:173], v[186:189], v[108:111]
	ds_read_b128 v[198:201], v162 offset:10240
	ds_write_b64 v161, v[2:3] offset:43520
	v_mfma_f32_16x16x32_bf16 v[104:107], v[174:177], v[186:189], v[104:107]
	v_mfma_f32_16x16x32_bf16 v[100:103], v[178:181], v[186:189], v[100:103]
	v_mfma_f32_16x16x32_bf16 v[0:3], v[182:185], v[186:189], v[96:99]
	s_nop 2
	buffer_load_dwordx4 v[96:99], v160, s[12:15], s15 offen
	s_waitcnt lgkmcnt(2)
	v_mfma_f32_16x16x32_bf16 v[92:95], v[170:173], v[190:193], v[92:95]
	ds_read_b128 v[186:189], v162 offset:12288
	v_mfma_f32_16x16x32_bf16 v[88:91], v[174:177], v[190:193], v[88:91]
	v_mfma_f32_16x16x32_bf16 v[84:87], v[178:181], v[190:193], v[84:87]
	v_mfma_f32_16x16x32_bf16 v[80:83], v[182:185], v[190:193], v[80:83]
	s_waitcnt vmcnt(11)
	v_cvt_pk_bf16_f32 v31, v30, v31
	v_cvt_pk_bf16_f32 v30, v28, v29
	s_waitcnt lgkmcnt(2)
	v_mfma_f32_16x16x32_bf16 v[76:79], v[170:173], v[198:201], v[76:79]
	ds_read_b128 v[190:193], v162 offset:14336
	ds_write_b64 v161, v[30:31] offset:52224
	v_mfma_f32_16x16x32_bf16 v[72:75], v[174:177], v[198:201], v[72:75]
	v_mfma_f32_16x16x32_bf16 v[68:71], v[178:181], v[198:201], v[68:71]
	v_mfma_f32_16x16x32_bf16 v[28:31], v[182:185], v[198:201], v[64:67]
	s_nop 2
	buffer_load_dwordx4 v[64:67], v160, s[12:15], s54 offen
	s_waitcnt lgkmcnt(2)
	v_mfma_f32_16x16x32_bf16 v[60:63], v[170:173], v[186:189], v[60:63]
	ds_read_b128 v[198:201], v162 offset:1024
	v_mfma_f32_16x16x32_bf16 v[56:59], v[174:177], v[186:189], v[56:59]
	v_mfma_f32_16x16x32_bf16 v[52:55], v[178:181], v[186:189], v[52:55]
	v_mfma_f32_16x16x32_bf16 v[48:51], v[182:185], v[186:189], v[48:51]
	s_waitcnt lgkmcnt(2)
	v_mfma_f32_16x16x32_bf16 v[44:47], v[170:173], v[190:193], v[44:47]
	ds_read_b128 v[170:173], v162 offset:3072
	v_mfma_f32_16x16x32_bf16 v[40:43], v[174:177], v[190:193], v[40:43]
	ds_read_b64_tr_b16 v[174:175], v166 offset:17408
	ds_read_b64_tr_b16 v[186:187], v166 offset:17440
	ds_read_b64_tr_b16 v[202:203], v166 offset:17472
	ds_read_b64_tr_b16 v[206:207], v166 offset:17504
	ds_read_b64_tr_b16 v[176:177], v167 offset:17408
	ds_read_b64_tr_b16 v[188:189], v167 offset:17440
	ds_read_b64_tr_b16 v[204:205], v167 offset:17472
	ds_read_b64_tr_b16 v[208:209], v167 offset:17504
	v_mfma_f32_16x16x32_bf16 v[36:39], v[178:181], v[190:193], v[36:39]
	s_waitcnt vmcnt(11)
	v_cvt_pk_bf16_f32 v179, v26, v27
	v_cvt_pk_bf16_f32 v178, v24, v25
	ds_write_b64 v161, v[178:179] offset:60928
	v_mfma_f32_16x16x32_bf16 v[24:27], v[182:185], v[190:193], v[32:35]
	s_nop 2
	buffer_load_dwordx4 v[32:35], v160, s[12:15], s55 offen
	s_waitcnt lgkmcnt(3)
	v_mfma_f32_16x16x32_bf16 v[152:155], v[186:189], v[198:201], v[152:155]
	ds_read_b128 v[178:181], v162 offset:5120
	s_waitcnt lgkmcnt(3)
	v_mfma_f32_16x16x32_bf16 v[148:151], v[202:205], v[198:201], v[148:151]
	s_waitcnt lgkmcnt(2)
; #define G_ENDTILE(VM) do { asm volatile("s_waitcnt vmcnt(" #VM ")" ::: "memory"); \
;         asm volatile("s_waitcnt lgkmcnt(0)" ::: "memory"); __builtin_amdgcn_s_barrier(); asm volatile("" ::: "memory"); } while (0)
;     ...
;         G_TILE(G_A1, G_B1, true, G_B0, G_A0, 0, true, 1, (void)0);
;         G_ENDTILE(8);
	v_mfma_f32_16x16x32_bf16 v[144:147], v[206:209], v[198:201], v[144:147]
	v_mfma_f32_16x16x32_bf16 v[156:159], v[174:177], v[198:201], v[156:159]
	v_mfma_f32_16x16x32_bf16 v[140:143], v[174:177], v[170:173], v[140:143]
	ds_read_b128 v[182:185], v162 offset:7168
	s_waitcnt vmcnt(11)
	v_cvt_pk_bf16_f32 v23, v22, v23
	v_cvt_pk_bf16_f32 v22, v20, v21
	v_mfma_f32_16x16x32_bf16 v[136:139], v[186:189], v[170:173], v[136:139]
	ds_write_b64 v161, v[22:23] offset:35072
	v_mfma_f32_16x16x32_bf16 v[132:135], v[202:205], v[170:173], v[132:135]
	v_mfma_f32_16x16x32_bf16 v[12:15], v[206:209], v[170:173], v[12:15]
	buffer_load_dwordx4 v[20:23], v160, s[16:19], 0 offen
	s_waitcnt lgkmcnt(2)
	v_mfma_f32_16x16x32_bf16 v[124:127], v[174:177], v[178:181], v[124:127]
	ds_read_b128 v[170:173], v162 offset:9216
	v_mfma_f32_16x16x32_bf16 v[120:123], v[186:189], v[178:181], v[120:123]
	v_mfma_f32_16x16x32_bf16 v[116:119], v[202:205], v[178:181], v[116:119]
	v_mfma_f32_16x16x32_bf16 v[112:115], v[206:209], v[178:181], v[112:115]
	s_waitcnt lgkmcnt(2)
	v_mfma_f32_16x16x32_bf16 v[108:111], v[174:177], v[182:185], v[108:111]
	ds_read_b128 v[178:181], v162 offset:11264
	s_waitcnt vmcnt(11)
	v_cvt_pk_bf16_f32 v7, v6, v7
	v_cvt_pk_bf16_f32 v6, v4, v5
	v_mfma_f32_16x16x32_bf16 v[104:107], v[186:189], v[182:185], v[104:107]
	ds_write_b64 v161, v[6:7] offset:43776
	v_mfma_f32_16x16x32_bf16 v[100:103], v[202:205], v[182:185], v[100:103]
	v_mfma_f32_16x16x32_bf16 v[0:3], v[206:209], v[182:185], v[0:3]
	buffer_load_dwordx4 v[4:7], v160, s[16:19], s15 offen
	s_waitcnt lgkmcnt(2)
	v_mfma_f32_16x16x32_bf16 v[92:95], v[174:177], v[170:173], v[92:95]
	ds_read_b128 v[182:185], v162 offset:13312
	v_mfma_f32_16x16x32_bf16 v[88:91], v[186:189], v[170:173], v[88:91]
	v_mfma_f32_16x16x32_bf16 v[84:87], v[202:205], v[170:173], v[84:87]
	v_mfma_f32_16x16x32_bf16 v[80:83], v[206:209], v[170:173], v[80:83]
	s_waitcnt vmcnt(11)
	v_cvt_pk_bf16_f32 v11, v10, v11
	v_cvt_pk_bf16_f32 v10, v8, v9
	s_waitcnt lgkmcnt(2)
	v_mfma_f32_16x16x32_bf16 v[76:79], v[174:177], v[178:181], v[76:79]
	ds_read_b128 v[170:173], v162 offset:15360
	ds_write_b64 v161, v[10:11] offset:52480
	v_mfma_f32_16x16x32_bf16 v[72:75], v[186:189], v[178:181], v[72:75]
	v_mfma_f32_16x16x32_bf16 v[68:71], v[202:205], v[178:181], v[68:71]
	v_mfma_f32_16x16x32_bf16 v[8:11], v[206:209], v[178:181], v[28:31]
	buffer_load_dwordx4 v[178:181], v160, s[16:19], s54 offen
	s_waitcnt lgkmcnt(2)
	v_mfma_f32_16x16x32_bf16 v[60:63], v[174:177], v[182:185], v[60:63]
	v_mfma_f32_16x16x32_bf16 v[56:59], v[186:189], v[182:185], v[56:59]
	v_mfma_f32_16x16x32_bf16 v[52:55], v[202:205], v[182:185], v[52:55]
	v_mfma_f32_16x16x32_bf16 v[48:51], v[206:209], v[182:185], v[48:51]
	s_waitcnt vmcnt(11)
	v_cvt_pk_bf16_f32 v19, v18, v19
	v_cvt_pk_bf16_f32 v18, v16, v17
	s_waitcnt lgkmcnt(1)
	v_mfma_f32_16x16x32_bf16 v[44:47], v[174:177], v[170:173], v[44:47]
	ds_write_b64 v161, v[18:19] offset:61184
	v_mfma_f32_16x16x32_bf16 v[40:43], v[186:189], v[170:173], v[40:43]
	v_mfma_f32_16x16x32_bf16 v[36:39], v[202:205], v[170:173], v[36:39]
	v_mfma_f32_16x16x32_bf16 v[16:19], v[206:209], v[170:173], v[24:27]
	buffer_load_dwordx4 v[170:173], v160, s[16:19], s55 offen
	s_waitcnt vmcnt(8)
	s_mov_b32 m0, s56
	s_waitcnt lgkmcnt(0)
	s_barrier
	ds_read_b64_tr_b16 v[24:25], v166 offset:34816
	ds_read_b64_tr_b16 v[26:27], v167 offset:34816
	ds_read_b64_tr_b16 v[176:177], v167 offset:34848
	ds_read_b128 v[28:31], v162 offset:32768
	ds_read_b64_tr_b16 v[174:175], v166 offset:34848
	ds_read_b64_tr_b16 v[182:183], v166 offset:34880
	ds_read_b64_tr_b16 v[186:187], v166 offset:34912
	ds_read_b64_tr_b16 v[184:185], v167 offset:34880
	ds_read_b64_tr_b16 v[188:189], v167 offset:34912
	ds_read_b128 v[190:193], v162 offset:34816
	ds_read_b128 v[198:201], v162 offset:36864
	buffer_load_dwordx4 v163, s[20:23], 0 offen lds
	s_mov_b32 m0, s57
	s_waitcnt lgkmcnt(6)
	v_mfma_f32_16x16x32_bf16 v[152:155], v[174:177], v[28:31], v[152:155]
	buffer_load_dwordx4 v165, s[20:23], 0 offen lds
	s_mov_b32 m0, s58
	s_nop 0
	buffer_load_dwordx4 v164, s[20:23], 0 offen lds
	s_mov_b32 m0, s59
	s_waitcnt lgkmcnt(3)
	v_mfma_f32_16x16x32_bf16 v[148:151], v[182:185], v[28:31], v[148:151]
	buffer_load_dwordx4 v168, s[20:23], 0 offen lds
	s_waitcnt lgkmcnt(2)
	v_mfma_f32_16x16x32_bf16 v[144:147], v[186:189], v[28:31], v[144:147]
	v_mfma_f32_16x16x32_bf16 v[156:159], v[24:27], v[28:31], v[156:159]
	ds_read_b128 v[28:31], v162 offset:38912
	s_waitcnt lgkmcnt(2)
	v_mfma_f32_16x16x32_bf16 v[140:143], v[24:27], v[190:193], v[140:143]
	s_waitcnt vmcnt(11)
	v_cvt_pk_bf16_f32 v131, v130, v131
	v_cvt_pk_bf16_f32 v130, v128, v129
	ds_write_b64 v161, v[130:131]
	v_mfma_f32_16x16x32_bf16 v[136:139], v[174:177], v[190:193], v[136:139]
	v_mfma_f32_16x16x32_bf16 v[202:205], v[182:185], v[190:193], v[132:135]
	v_mfma_f32_16x16x32_bf16 v[190:193], v[186:189], v[190:193], v[12:15]
	s_nop 2
	buffer_load_dwordx4 v[12:15], v160, s[12:15], s38 offen
	ds_read_b128 v[128:131], v162 offset:40960
	s_waitcnt lgkmcnt(3)
	v_mfma_f32_16x16x32_bf16 v[124:127], v[24:27], v[198:201], v[124:127]
	v_mfma_f32_16x16x32_bf16 v[120:123], v[174:177], v[198:201], v[120:123]
	v_mfma_f32_16x16x32_bf16 v[116:119], v[182:185], v[198:201], v[116:119]
	v_mfma_f32_16x16x32_bf16 v[198:201], v[186:189], v[198:201], v[112:115]
	s_nop 2
	ds_read_b128 v[112:115], v162 offset:43008
	s_waitcnt lgkmcnt(3)
	v_mfma_f32_16x16x32_bf16 v[108:111], v[24:27], v[28:31], v[108:111]
	s_waitcnt vmcnt(11)
; DI int lane_id() { int l; asm volatile("v_mbcnt_lo_u32_b32 %0, -1, 0\n\tv_mbcnt_hi_u32_b32 %0, -1, %0" : "=v"(l)); return l; }
; #define G_ENDTILE(VM) do { asm volatile("s_waitcnt vmcnt(" #VM ")" ::: "memory"); \
;         asm volatile("s_waitcnt lgkmcnt(0)" ::: "memory"); __builtin_amdgcn_s_barrier(); asm volatile("" ::: "memory"); } while (0)
;     ...
;         G_TILE(G_A1, G_B1, true, G_B0, G_A0, 0, true, 1, (void)0);
;         G_ENDTILE(8);
;         { const int l2 = lane_id(); cur.ep(acc, wr, wc, l2 & 15, l2 >> 4); }
	v_cvt_pk_bf16_f32 v99, v98, v99
	v_cvt_pk_bf16_f32 v98, v96, v97
	ds_write_b64 v161, v[98:99] offset:8704
	v_mfma_f32_16x16x32_bf16 v[104:107], v[174:177], v[28:31], v[104:107]
	v_mfma_f32_16x16x32_bf16 v[206:209], v[182:185], v[28:31], v[100:103]
	v_mfma_f32_16x16x32_bf16 v[210:213], v[186:189], v[28:31], v[0:3]
	s_nop 2
	buffer_load_dwordx4 v[0:3], v160, s[12:15], s39 offen
	ds_read_b128 v[96:99], v162 offset:45056
	s_waitcnt lgkmcnt(3)
	v_mfma_f32_16x16x32_bf16 v[92:95], v[24:27], v[128:131], v[92:95]
	v_mfma_f32_16x16x32_bf16 v[88:91], v[174:177], v[128:131], v[88:91]
	v_mfma_f32_16x16x32_bf16 v[84:87], v[182:185], v[128:131], v[84:87]
	v_mfma_f32_16x16x32_bf16 v[214:217], v[186:189], v[128:131], v[80:83]
	s_nop 2
	ds_read_b128 v[80:83], v162 offset:47104
	s_waitcnt lgkmcnt(3)
	v_mfma_f32_16x16x32_bf16 v[76:79], v[24:27], v[112:115], v[76:79]
	s_waitcnt vmcnt(11)
	v_cvt_pk_bf16_f32 v29, v66, v67
	v_cvt_pk_bf16_f32 v28, v64, v65
	ds_write_b64 v161, v[28:29] offset:17408
	v_mfma_f32_16x16x32_bf16 v[72:75], v[174:177], v[112:115], v[72:75]
	v_mfma_f32_16x16x32_bf16 v[8:11], v[186:189], v[112:115], v[8:11]
	v_mfma_f32_16x16x32_bf16 v[218:221], v[182:185], v[112:115], v[68:71]
	buffer_load_dwordx4 v[28:31], v160, s[12:15], s60 offen
	ds_read_b128 v[64:67], v162 offset:33792
	s_waitcnt lgkmcnt(3)
	v_mfma_f32_16x16x32_bf16 v[60:63], v[24:27], v[96:99], v[60:63]
	v_mfma_f32_16x16x32_bf16 v[56:59], v[174:177], v[96:99], v[56:59]
	v_mfma_f32_16x16x32_bf16 v[52:55], v[182:185], v[96:99], v[52:55]
	v_mfma_f32_16x16x32_bf16 v[48:51], v[186:189], v[96:99], v[48:51]
	ds_read_b128 v[68:71], v162 offset:35840
	s_waitcnt lgkmcnt(3)
	v_mfma_f32_16x16x32_bf16 v[40:43], v[174:177], v[80:83], v[40:43]
	ds_read_b64_tr_b16 v[174:175], v166 offset:52224
	ds_read_b64_tr_b16 v[222:223], v166 offset:52256
	ds_read_b64_tr_b16 v[226:227], v166 offset:52288
	ds_read_b64_tr_b16 v[230:231], v166 offset:52320
	ds_read_b64_tr_b16 v[176:177], v167 offset:52224
	ds_read_b64_tr_b16 v[224:225], v167 offset:52256
	ds_read_b64_tr_b16 v[228:229], v167 offset:52288
	ds_read_b64_tr_b16 v[232:233], v167 offset:52320
	v_mfma_f32_16x16x32_bf16 v[44:47], v[24:27], v[80:83], v[44:47]
	s_waitcnt vmcnt(11)
	v_cvt_pk_bf16_f32 v25, v34, v35
	v_cvt_pk_bf16_f32 v24, v32, v33
	ds_write_b64 v161, v[24:25] offset:26112
	v_mfma_f32_16x16x32_bf16 v[16:19], v[186:189], v[80:83], v[16:19]
	v_mfma_f32_16x16x32_bf16 v[182:185], v[182:185], v[80:83], v[36:39]
	buffer_load_dwordx4 v[24:27], v160, s[12:15], s61 offen
	ds_read_b128 v[32:35], v162 offset:37888
	s_waitcnt lgkmcnt(5)
	v_mfma_f32_16x16x32_bf16 v[156:159], v[174:177], v[64:67], v[156:159]
	s_waitcnt lgkmcnt(4)
	v_mfma_f32_16x16x32_bf16 v[186:189], v[222:225], v[64:67], v[152:155]
	s_waitcnt lgkmcnt(3)
	v_mfma_f32_16x16x32_bf16 v[234:237], v[226:229], v[64:67], v[148:151]
	s_waitcnt lgkmcnt(2)
	v_mfma_f32_16x16x32_bf16 v[238:241], v[230:233], v[64:67], v[144:147]
	ds_read_b128 v[36:39], v162 offset:39936
	v_mfma_f32_16x16x32_bf16 v[140:143], v[174:177], v[68:71], v[140:143]
	s_waitcnt vmcnt(11)
	v_cvt_pk_bf16_f32 v23, v22, v23
	v_cvt_pk_bf16_f32 v22, v20, v21
	ds_write_b64 v161, v[22:23] offset:256
	v_mfma_f32_16x16x32_bf16 v[132:135], v[222:225], v[68:71], v[136:139]
	v_mfma_f32_16x16x32_bf16 v[128:131], v[226:229], v[68:71], v[202:205]
	v_mfma_f32_16x16x32_bf16 v[136:139], v[230:233], v[68:71], v[190:193]
	buffer_load_dwordx4 v[20:23], v160, s[16:19], s38 offen
	ds_read_b128 v[64:67], v162 offset:41984
	s_waitcnt lgkmcnt(3)
	v_mfma_f32_16x16x32_bf16 v[124:127], v[174:177], v[32:35], v[124:127]
	v_mfma_f32_16x16x32_bf16 v[120:123], v[222:225], v[32:35], v[120:123]
	v_mfma_f32_16x16x32_bf16 v[112:115], v[226:229], v[32:35], v[116:119]
	v_mfma_f32_16x16x32_bf16 v[116:119], v[230:233], v[32:35], v[198:201]
	ds_read_b128 v[32:35], v162 offset:44032
	s_waitcnt lgkmcnt(3)
	v_mfma_f32_16x16x32_bf16 v[108:111], v[174:177], v[36:39], v[108:111]
	s_waitcnt vmcnt(11)
	v_cvt_pk_bf16_f32 v7, v6, v7
	v_cvt_pk_bf16_f32 v6, v4, v5
	ds_write_b64 v161, v[6:7] offset:8960
	v_mfma_f32_16x16x32_bf16 v[100:103], v[222:225], v[36:39], v[104:107]
	v_mfma_f32_16x16x32_bf16 v[96:99], v[226:229], v[36:39], v[206:209]
	v_mfma_f32_16x16x32_bf16 v[104:107], v[230:233], v[36:39], v[210:213]
	buffer_load_dwordx4 v[4:7], v160, s[16:19], s39 offen
	ds_read_b128 v[36:39], v162 offset:46080
	s_waitcnt lgkmcnt(3)
	v_mfma_f32_16x16x32_bf16 v[92:95], v[174:177], v[64:67], v[92:95]
	v_mfma_f32_16x16x32_bf16 v[88:91], v[222:225], v[64:67], v[88:91]
	v_mfma_f32_16x16x32_bf16 v[80:83], v[226:229], v[64:67], v[84:87]
	v_mfma_f32_16x16x32_bf16 v[84:87], v[230:233], v[64:67], v[214:217]
	s_waitcnt lgkmcnt(2)
	v_mfma_f32_16x16x32_bf16 v[68:71], v[222:225], v[32:35], v[72:75]
	ds_read_b128 v[144:147], v162 offset:48128
	s_waitcnt vmcnt(11)
	s_nop 0
	v_cvt_pk_bf16_f32 v73, v180, v181
	v_cvt_pk_bf16_f32 v72, v178, v179
	v_mfma_f32_16x16x32_bf16 v[76:79], v[174:177], v[32:35], v[76:79]
	ds_write_b64 v161, v[72:73] offset:17664
	v_mfma_f32_16x16x32_bf16 v[64:67], v[226:229], v[32:35], v[218:221]
	v_mfma_f32_16x16x32_bf16 v[72:75], v[230:233], v[32:35], v[8:11]
	s_nop 2
	buffer_load_dwordx4 v[8:11], v160, s[16:19], s60 offen
	s_waitcnt lgkmcnt(2)
	v_mfma_f32_16x16x32_bf16 v[60:63], v[174:177], v[36:39], v[60:63]
	v_mfma_f32_16x16x32_bf16 v[56:59], v[222:225], v[36:39], v[56:59]
	v_mfma_f32_16x16x32_bf16 v[52:55], v[226:229], v[36:39], v[52:55]
	v_mfma_f32_16x16x32_bf16 v[48:51], v[230:233], v[36:39], v[48:51]
	s_waitcnt lgkmcnt(1)
	v_mfma_f32_16x16x32_bf16 v[36:39], v[222:225], v[144:147], v[40:43]
	s_waitcnt vmcnt(11)
	s_nop 1
	v_cvt_pk_bf16_f32 v41, v172, v173
	v_cvt_pk_bf16_f32 v40, v170, v171
	v_mfma_f32_16x16x32_bf16 v[44:47], v[174:177], v[144:147], v[44:47]
	ds_write_b64 v161, v[40:41] offset:26368
	v_mfma_f32_16x16x32_bf16 v[32:35], v[226:229], v[144:147], v[182:185]
	v_mfma_f32_16x16x32_bf16 v[40:43], v[230:233], v[144:147], v[16:19]
	s_nop 2
	buffer_load_dwordx4 v[16:19], v160, s[16:19], s61 offen
	v_and_b32_e32 v148, 64, v169
	v_xor_b32_e32 v147, 16, v169
	v_add_u32_e32 v148, 64, v148
	v_cmp_lt_i32_e32 vcc, v147, v148
	s_waitcnt vmcnt(8)
	s_waitcnt lgkmcnt(0)
	s_barrier
	v_mbcnt_lo_u32_b32 v146, -1, 0
	v_mbcnt_hi_u32_b32 v146, -1, v146
	s_nop 0
	v_cndmask_b32_e32 v147, v169, v147, vcc
	v_lshlrev_b32_e32 v151, 2, v147
	v_xor_b32_e32 v147, 32, v169
	v_and_or_b32 v152, v146, 15, s66
	v_cmp_lt_i32_e32 vcc, v147, v148
	v_ashrrev_i32_e32 v144, 1, v146
	s_lshl_b32 s18, s49, 8
	v_cndmask_b32_e32 v147, v169, v147, vcc
	v_cmp_gt_u32_e32 vcc, 16, v146
	v_add_u32_e32 v146, s68, v152
	v_lshlrev_b32_e32 v150, 2, v147
	v_ashrrev_i32_e32 v147, 31, v146
	v_lshlrev_b64 v[148:149], 12, v[146:147]
	v_mul_f32_e32 v154, v187, v187
	v_mul_f32_e32 v155, v189, v189
	v_lshl_add_u64 v[148:149], s[40:41], 0, v[148:149]
	s_ashr_i32 s19, s18, 31
	v_fmac_f32_e32 v154, v186, v186
	v_fmac_f32_e32 v155, v188, v188
	v_and_b32_e32 v144, -8, v144
	v_lshl_add_u64 v[148:149], s[18:19], 1, v[148:149]
	v_mul_f32_e32 v153, v157, v157
	v_mul_f32_e32 v172, v159, v159
	v_add_f32_e32 v173, v154, v155
	v_mul_f32_e32 v154, v235, v235
	v_mul_f32_e32 v155, v237, v237
	v_ashrrev_i32_e32 v145, 31, v144
	v_lshl_add_u64 v[148:149], v[148:149], 0, s[36:37]
	v_fmac_f32_e32 v172, v158, v158
	v_fmac_f32_e32 v154, v234, v234
	v_fmac_f32_e32 v155, v236, v236
	v_fmac_f32_e32 v153, v156, v156
	v_add_f32_e32 v174, v154, v155
	v_mul_f32_e32 v154, v239, v239
	v_mul_f32_e32 v155, v241, v241
	v_lshl_add_u64 v[170:171], v[144:145], 1, v[148:149]
	v_add_f32_e32 v148, v153, v172
	v_fmac_f32_e32 v154, v238, v238
	v_fmac_f32_e32 v155, v240, v240
	v_add_f32_e32 v148, v148, v173
	v_add_f32_e32 v175, v154, v155
	v_add_f32_e32 v148, v148, v174
	v_add_f32_e32 v148, v148, v175
	v_mov_b32_e32 v149, v148
	s_nop 1
	v_permlane16_swap_b32 v148, v149
	v_cvt_pk_bf16_f32 v155, v158, v159
	v_cvt_pk_bf16_f32 v154, v156, v157
	v_cvt_pk_bf16_f32 v157, v188, v189
	v_cvt_pk_bf16_f32 v156, v186, v187
	s_waitcnt lgkmcnt(0)
	v_add_f32_e32 v148, v148, v149
	v_mov_b32_e32 v149, v148
	s_nop 1
	v_permlane32_swap_b32 v148, v149
	global_store_dwordx4 v[170:171], v[154:157], off
	s_nop 1
	v_cvt_pk_bf16_f32 v155, v236, v237
	v_cvt_pk_bf16_f32 v154, v234, v235
	v_cvt_pk_bf16_f32 v157, v240, v241
	v_cvt_pk_bf16_f32 v156, v238, v239
	global_store_dwordx4 v[170:171], v[154:157], off offset:64
	s_and_saveexec_b64 s[22:23], vcc
	s_cbranch_execz .LBB0_905
	s_waitcnt lgkmcnt(0)
	v_add_f32_e32 v153, v148, v149
	s_lshl_b32 s74, s49, 2
	v_lshlrev_b64 v[148:149], 7, v[146:147]
	s_ashr_i32 s75, s74, 31
	v_lshl_add_u64 v[148:149], s[42:43], 0, v[148:149]
	v_lshl_add_u64 v[148:149], s[74:75], 2, v[148:149]
	s_lshl_b32 s74, s73, 2
	s_mov_b32 s75, s37
	v_lshl_add_u64 v[148:149], v[148:149], 0, s[74:75]
	global_store_dword v[148:149], v153, off
.LBB0_905:
	s_or_b64 exec, exec, s[22:23]
	v_add3_u32 v148, v152, s68, 16
	v_mul_f32_e32 v156, v133, v133
	v_mul_f32_e32 v157, v135, v135
	s_waitcnt lgkmcnt(0)
	v_ashrrev_i32_e32 v149, 31, v148
	v_fmac_f32_e32 v156, v132, v132
	v_fmac_f32_e32 v157, v134, v134
	v_lshlrev_b64 v[154:155], 12, v[148:149]
	v_add_f32_e32 v156, v156, v157
	v_mul_f32_e32 v157, v129, v129
	v_mul_f32_e32 v158, v131, v131
	v_lshl_add_u64 v[154:155], s[40:41], 0, v[154:155]
	v_fmac_f32_e32 v157, v128, v128
	v_fmac_f32_e32 v158, v130, v130
	v_lshl_add_u64 v[154:155], s[18:19], 1, v[154:155]
	v_mul_f32_e32 v147, v141, v141
	v_mul_f32_e32 v153, v143, v143
	v_add_f32_e32 v157, v157, v158
	v_mul_f32_e32 v158, v137, v137
	v_mul_f32_e32 v159, v139, v139
	v_lshl_add_u64 v[154:155], v[154:155], 0, s[36:37]
	v_fmac_f32_e32 v153, v142, v142
	v_fmac_f32_e32 v158, v136, v136
	v_fmac_f32_e32 v159, v138, v138
	v_fmac_f32_e32 v147, v140, v140
	v_add_f32_e32 v170, v158, v159
	v_lshl_add_u64 v[158:159], v[144:145], 1, v[154:155]
	v_cvt_pk_bf16_f32 v154, v140, v141
	v_add_f32_e32 v140, v147, v153
	v_add_f32_e32 v140, v140, v156
	v_add_f32_e32 v140, v140, v157
	v_add_f32_e32 v140, v140, v170
	v_mov_b32_e32 v141, v140
	s_nop 1
	v_permlane16_swap_b32 v140, v141
	v_cvt_pk_bf16_f32 v156, v132, v133
	v_cvt_pk_bf16_f32 v133, v130, v131
	v_cvt_pk_bf16_f32 v155, v142, v143
	v_cvt_pk_bf16_f32 v157, v134, v135
	s_waitcnt lgkmcnt(0)
	v_add_f32_e32 v130, v140, v141
	v_mov_b32_e32 v131, v130
	s_nop 1
	v_permlane32_swap_b32 v130, v131
	v_cvt_pk_bf16_f32 v132, v128, v129
	v_cvt_pk_bf16_f32 v135, v138, v139
	v_cvt_pk_bf16_f32 v134, v136, v137
	global_store_dwordx4 v[158:159], v[154:157], off
	global_store_dwordx4 v[158:159], v[132:135], off offset:64
	s_and_saveexec_b64 s[22:23], vcc
	s_cbranch_execz .LBB0_907
	s_lshl_b32 s74, s49, 2
	v_lshlrev_b64 v[128:129], 7, v[148:149]
	s_ashr_i32 s75, s74, 31
	v_lshl_add_u64 v[128:129], s[42:43], 0, v[128:129]
	v_lshl_add_u64 v[128:129], s[74:75], 2, v[128:129]
	s_lshl_b32 s74, s73, 2
	s_mov_b32 s75, s37
	s_waitcnt lgkmcnt(0)
	v_add_f32_e32 v130, v130, v131
	v_lshl_add_u64 v[128:129], v[128:129], 0, s[74:75]
	global_store_dword v[128:129], v130, off
.LBB0_907:
	s_or_b64 exec, exec, s[22:23]
	v_add3_u32 v128, v152, s68, 32
	v_mul_f32_e32 v134, v121, v121
	v_mul_f32_e32 v135, v123, v123
	v_ashrrev_i32_e32 v129, 31, v128
	v_fmac_f32_e32 v134, v120, v120
	v_fmac_f32_e32 v135, v122, v122
	s_waitcnt lgkmcnt(0)
	v_lshlrev_b64 v[130:131], 12, v[128:129]
	v_add_f32_e32 v136, v134, v135
	v_mul_f32_e32 v134, v113, v113
	v_mul_f32_e32 v135, v115, v115
	v_lshl_add_u64 v[130:131], s[40:41], 0, v[130:131]
	v_fmac_f32_e32 v134, v112, v112
	v_fmac_f32_e32 v135, v114, v114
	v_lshl_add_u64 v[130:131], s[18:19], 1, v[130:131]
	v_mul_f32_e32 v132, v125, v125
	v_mul_f32_e32 v133, v127, v127
	v_add_f32_e32 v137, v134, v135
	v_mul_f32_e32 v134, v117, v117
	v_mul_f32_e32 v135, v119, v119
	v_lshl_add_u64 v[130:131], v[130:131], 0, s[36:37]
	v_fmac_f32_e32 v133, v126, v126
	v_fmac_f32_e32 v134, v116, v116
	v_fmac_f32_e32 v135, v118, v118
	v_fmac_f32_e32 v132, v124, v124
	v_add_f32_e32 v138, v134, v135
	v_lshl_add_u64 v[134:135], v[144:145], 1, v[130:131]
	v_cvt_pk_bf16_f32 v130, v124, v125
	v_add_f32_e32 v124, v132, v133
	v_add_f32_e32 v124, v124, v136
	v_add_f32_e32 v124, v124, v137
	v_add_f32_e32 v124, v124, v138
	v_mov_b32_e32 v125, v124
	s_nop 1
	v_permlane16_swap_b32 v124, v125
	v_cvt_pk_bf16_f32 v132, v120, v121
	v_cvt_pk_bf16_f32 v121, v114, v115
	v_cvt_pk_bf16_f32 v131, v126, v127
	v_cvt_pk_bf16_f32 v133, v122, v123
	s_waitcnt lgkmcnt(0)
	v_add_f32_e32 v114, v124, v125
	v_mov_b32_e32 v115, v114
	s_nop 1
	v_permlane32_swap_b32 v114, v115
	v_cvt_pk_bf16_f32 v120, v112, v113
	v_cvt_pk_bf16_f32 v123, v118, v119
	v_cvt_pk_bf16_f32 v122, v116, v117
	global_store_dwordx4 v[134:135], v[130:133], off
	global_store_dwordx4 v[134:135], v[120:123], off offset:64
	s_and_saveexec_b64 s[22:23], vcc
	s_cbranch_execz .LBB0_909
	s_lshl_b32 s74, s49, 2
	v_lshlrev_b64 v[112:113], 7, v[128:129]
	s_ashr_i32 s75, s74, 31
	v_lshl_add_u64 v[112:113], s[42:43], 0, v[112:113]
	v_lshl_add_u64 v[112:113], s[74:75], 2, v[112:113]
	s_lshl_b32 s74, s73, 2
	s_mov_b32 s75, s37
	s_waitcnt lgkmcnt(0)
	v_add_f32_e32 v114, v114, v115
	v_lshl_add_u64 v[112:113], v[112:113], 0, s[74:75]
	global_store_dword v[112:113], v114, off
.LBB0_909:
	s_or_b64 exec, exec, s[22:23]
	v_add3_u32 v112, v152, s68, 48
	v_mul_f32_e32 v118, v101, v101
	v_mul_f32_e32 v119, v103, v103
	v_ashrrev_i32_e32 v113, 31, v112
	v_fmac_f32_e32 v118, v100, v100
	v_fmac_f32_e32 v119, v102, v102
	s_waitcnt lgkmcnt(0)
	v_lshlrev_b64 v[114:115], 12, v[112:113]
	v_add_f32_e32 v120, v118, v119
	v_mul_f32_e32 v118, v97, v97
	v_mul_f32_e32 v119, v99, v99
	v_lshl_add_u64 v[114:115], s[40:41], 0, v[114:115]
	v_fmac_f32_e32 v118, v96, v96
	v_fmac_f32_e32 v119, v98, v98
	v_lshl_add_u64 v[114:115], s[18:19], 1, v[114:115]
	v_mul_f32_e32 v116, v109, v109
	v_mul_f32_e32 v117, v111, v111
	v_add_f32_e32 v121, v118, v119
	v_mul_f32_e32 v118, v105, v105
	v_mul_f32_e32 v119, v107, v107
	v_lshl_add_u64 v[114:115], v[114:115], 0, s[36:37]
	v_fmac_f32_e32 v117, v110, v110
	v_fmac_f32_e32 v118, v104, v104
	v_fmac_f32_e32 v119, v106, v106
	v_fmac_f32_e32 v116, v108, v108
	v_add_f32_e32 v122, v118, v119
	v_lshl_add_u64 v[118:119], v[144:145], 1, v[114:115]
	v_cvt_pk_bf16_f32 v114, v108, v109
	v_add_f32_e32 v108, v116, v117
	v_add_f32_e32 v108, v108, v120
	v_add_f32_e32 v108, v108, v121
	v_add_f32_e32 v108, v108, v122
	v_mov_b32_e32 v109, v108
	s_nop 1
	v_permlane16_swap_b32 v108, v109
	v_cvt_pk_bf16_f32 v116, v100, v101
	v_cvt_pk_bf16_f32 v101, v98, v99
	v_cvt_pk_bf16_f32 v115, v110, v111
	v_cvt_pk_bf16_f32 v117, v102, v103
	s_waitcnt lgkmcnt(0)
	v_add_f32_e32 v98, v108, v109
	v_mov_b32_e32 v99, v98
	s_nop 1
	v_permlane32_swap_b32 v98, v99
	v_cvt_pk_bf16_f32 v100, v96, v97
	v_cvt_pk_bf16_f32 v103, v106, v107
	v_cvt_pk_bf16_f32 v102, v104, v105
	global_store_dwordx4 v[118:119], v[114:117], off
	global_store_dwordx4 v[118:119], v[100:103], off offset:64
	s_and_saveexec_b64 s[22:23], vcc
	s_cbranch_execz .LBB0_911
	s_lshl_b32 s74, s49, 2
	v_lshlrev_b64 v[96:97], 7, v[112:113]
	s_ashr_i32 s75, s74, 31
	v_lshl_add_u64 v[96:97], s[42:43], 0, v[96:97]
	v_lshl_add_u64 v[96:97], s[74:75], 2, v[96:97]
	s_lshl_b32 s74, s73, 2
	s_mov_b32 s75, s37
	s_waitcnt lgkmcnt(0)
	v_add_f32_e32 v98, v98, v99
	v_lshl_add_u64 v[96:97], v[96:97], 0, s[74:75]
	global_store_dword v[96:97], v98, off
.LBB0_911:
	s_or_b64 exec, exec, s[22:23]
	v_add3_u32 v96, v152, s68, 64
	v_mul_f32_e32 v102, v89, v89
	v_mul_f32_e32 v103, v91, v91
	v_ashrrev_i32_e32 v97, 31, v96
	v_fmac_f32_e32 v102, v88, v88
	v_fmac_f32_e32 v103, v90, v90
	s_waitcnt lgkmcnt(0)
	v_lshlrev_b64 v[98:99], 12, v[96:97]
	v_add_f32_e32 v104, v102, v103
	v_mul_f32_e32 v102, v81, v81
	v_mul_f32_e32 v103, v83, v83
	v_lshl_add_u64 v[98:99], s[40:41], 0, v[98:99]
	v_fmac_f32_e32 v102, v80, v80
	v_fmac_f32_e32 v103, v82, v82
	v_lshl_add_u64 v[98:99], s[18:19], 1, v[98:99]
	v_mul_f32_e32 v100, v93, v93
	v_mul_f32_e32 v101, v95, v95
	v_add_f32_e32 v105, v102, v103
	v_mul_f32_e32 v102, v85, v85
	v_mul_f32_e32 v103, v87, v87
	v_lshl_add_u64 v[98:99], v[98:99], 0, s[36:37]
	v_fmac_f32_e32 v101, v94, v94
	v_fmac_f32_e32 v102, v84, v84
	v_fmac_f32_e32 v103, v86, v86
	v_fmac_f32_e32 v100, v92, v92
	v_add_f32_e32 v106, v102, v103
	v_lshl_add_u64 v[102:103], v[144:145], 1, v[98:99]
	v_cvt_pk_bf16_f32 v98, v92, v93
	v_add_f32_e32 v92, v100, v101
	v_add_f32_e32 v92, v92, v104
	v_add_f32_e32 v92, v92, v105
	v_add_f32_e32 v92, v92, v106
	v_mov_b32_e32 v93, v92
	s_nop 1
	v_permlane16_swap_b32 v92, v93
	v_cvt_pk_bf16_f32 v100, v88, v89
	v_cvt_pk_bf16_f32 v89, v82, v83
	v_cvt_pk_bf16_f32 v99, v94, v95
	v_cvt_pk_bf16_f32 v101, v90, v91
	s_waitcnt lgkmcnt(0)
	v_add_f32_e32 v82, v92, v93
	v_mov_b32_e32 v83, v82
	s_nop 1
	v_permlane32_swap_b32 v82, v83
	v_cvt_pk_bf16_f32 v88, v80, v81
	v_cvt_pk_bf16_f32 v91, v86, v87
	v_cvt_pk_bf16_f32 v90, v84, v85
	global_store_dwordx4 v[102:103], v[98:101], off
	global_store_dwordx4 v[102:103], v[88:91], off offset:64
	s_and_saveexec_b64 s[22:23], vcc
	s_cbranch_execz .LBB0_913
	s_lshl_b32 s68, s49, 2
	v_lshlrev_b64 v[80:81], 7, v[96:97]
	s_ashr_i32 s69, s68, 31
	v_lshl_add_u64 v[80:81], s[42:43], 0, v[80:81]
	v_lshl_add_u64 v[80:81], s[68:69], 2, v[80:81]
	s_lshl_b32 s68, s73, 2
	s_mov_b32 s69, s37
	s_waitcnt lgkmcnt(0)
	v_add_f32_e32 v82, v82, v83
	v_lshl_add_u64 v[80:81], v[80:81], 0, s[68:69]
	global_store_dword v[80:81], v82, off
.LBB0_913:
	s_or_b64 exec, exec, s[22:23]
	v_add_u32_e32 v80, 0x50, v146
	v_mul_f32_e32 v86, v69, v69
	v_mul_f32_e32 v87, v71, v71
	v_ashrrev_i32_e32 v81, 31, v80
	v_fmac_f32_e32 v86, v68, v68
	v_fmac_f32_e32 v87, v70, v70
	s_waitcnt lgkmcnt(0)
	v_lshlrev_b64 v[82:83], 12, v[80:81]
	v_add_f32_e32 v88, v86, v87
	v_mul_f32_e32 v86, v65, v65
	v_mul_f32_e32 v87, v67, v67
	v_lshl_add_u64 v[82:83], s[40:41], 0, v[82:83]
	v_fmac_f32_e32 v86, v64, v64
	v_fmac_f32_e32 v87, v66, v66
	v_lshl_add_u64 v[82:83], s[18:19], 1, v[82:83]
	v_mul_f32_e32 v84, v77, v77
	v_mul_f32_e32 v85, v79, v79
	v_add_f32_e32 v89, v86, v87
	v_mul_f32_e32 v86, v73, v73
	v_mul_f32_e32 v87, v75, v75
	v_lshl_add_u64 v[82:83], v[82:83], 0, s[36:37]
	v_fmac_f32_e32 v85, v78, v78
	v_fmac_f32_e32 v86, v72, v72
	v_fmac_f32_e32 v87, v74, v74
	v_fmac_f32_e32 v84, v76, v76
	v_add_f32_e32 v90, v86, v87
	v_lshl_add_u64 v[86:87], v[144:145], 1, v[82:83]
	v_cvt_pk_bf16_f32 v82, v76, v77
	v_add_f32_e32 v76, v84, v85
	v_add_f32_e32 v76, v76, v88
	v_add_f32_e32 v76, v76, v89
	v_add_f32_e32 v76, v76, v90
	v_mov_b32_e32 v77, v76
	s_nop 1
	v_permlane16_swap_b32 v76, v77
	v_cvt_pk_bf16_f32 v84, v68, v69
	v_cvt_pk_bf16_f32 v69, v66, v67
	v_cvt_pk_bf16_f32 v83, v78, v79
	v_cvt_pk_bf16_f32 v85, v70, v71
	s_waitcnt lgkmcnt(0)
	v_add_f32_e32 v66, v76, v77
	v_mov_b32_e32 v67, v66
	s_nop 1
	v_permlane32_swap_b32 v66, v67
	v_cvt_pk_bf16_f32 v68, v64, v65
	v_cvt_pk_bf16_f32 v71, v74, v75
	v_cvt_pk_bf16_f32 v70, v72, v73
	global_store_dwordx4 v[86:87], v[82:85], off
	global_store_dwordx4 v[86:87], v[68:71], off offset:64
	s_and_saveexec_b64 s[22:23], vcc
	s_cbranch_execz .LBB0_915
	s_lshl_b32 s68, s49, 2
	v_lshlrev_b64 v[64:65], 7, v[80:81]
	s_ashr_i32 s69, s68, 31
	v_lshl_add_u64 v[64:65], s[42:43], 0, v[64:65]
	v_lshl_add_u64 v[64:65], s[68:69], 2, v[64:65]
	s_lshl_b32 s68, s73, 2
	s_mov_b32 s69, s37
	s_waitcnt lgkmcnt(0)
	v_add_f32_e32 v66, v66, v67
	v_lshl_add_u64 v[64:65], v[64:65], 0, s[68:69]
	global_store_dword v[64:65], v66, off
.LBB0_915:
	s_or_b64 exec, exec, s[22:23]
	v_add_u32_e32 v64, 0x60, v146
	v_mul_f32_e32 v70, v57, v57
	v_mul_f32_e32 v71, v59, v59
	v_ashrrev_i32_e32 v65, 31, v64
	v_fmac_f32_e32 v70, v56, v56
	v_fmac_f32_e32 v71, v58, v58
	s_waitcnt lgkmcnt(0)
	v_lshlrev_b64 v[66:67], 12, v[64:65]
	v_add_f32_e32 v72, v70, v71
	v_mul_f32_e32 v70, v53, v53
	v_mul_f32_e32 v71, v55, v55
	v_lshl_add_u64 v[66:67], s[40:41], 0, v[66:67]
	v_fmac_f32_e32 v70, v52, v52
	v_fmac_f32_e32 v71, v54, v54
	v_lshl_add_u64 v[66:67], s[18:19], 1, v[66:67]
	v_mul_f32_e32 v68, v61, v61
	v_mul_f32_e32 v69, v63, v63
	v_add_f32_e32 v73, v70, v71
	v_mul_f32_e32 v70, v49, v49
	v_mul_f32_e32 v71, v51, v51
	v_lshl_add_u64 v[66:67], v[66:67], 0, s[36:37]
	v_fmac_f32_e32 v69, v62, v62
	v_fmac_f32_e32 v70, v48, v48
	v_fmac_f32_e32 v71, v50, v50
	v_fmac_f32_e32 v68, v60, v60
	v_add_f32_e32 v74, v70, v71
	v_lshl_add_u64 v[70:71], v[144:145], 1, v[66:67]
	v_cvt_pk_bf16_f32 v66, v60, v61
	v_add_f32_e32 v60, v68, v69
	v_add_f32_e32 v60, v60, v72
	v_add_f32_e32 v60, v60, v73
	v_add_f32_e32 v60, v60, v74
	v_mov_b32_e32 v61, v60
	s_nop 1
	v_permlane16_swap_b32 v60, v61
	v_cvt_pk_bf16_f32 v68, v56, v57
	v_cvt_pk_bf16_f32 v57, v54, v55
	v_cvt_pk_bf16_f32 v67, v62, v63
	v_cvt_pk_bf16_f32 v69, v58, v59
	s_waitcnt lgkmcnt(0)
	v_add_f32_e32 v54, v60, v61
	v_mov_b32_e32 v55, v54
	s_nop 1
	v_permlane32_swap_b32 v54, v55
	v_cvt_pk_bf16_f32 v56, v52, v53
	v_cvt_pk_bf16_f32 v59, v50, v51
	v_cvt_pk_bf16_f32 v58, v48, v49
	global_store_dwordx4 v[70:71], v[66:69], off
	global_store_dwordx4 v[70:71], v[56:59], off offset:64
	s_and_saveexec_b64 s[22:23], vcc
	s_cbranch_execz .LBB0_917
	s_lshl_b32 s68, s49, 2
	v_lshlrev_b64 v[48:49], 7, v[64:65]
	s_ashr_i32 s69, s68, 31
	v_lshl_add_u64 v[48:49], s[42:43], 0, v[48:49]
	v_lshl_add_u64 v[48:49], s[68:69], 2, v[48:49]
	s_lshl_b32 s68, s73, 2
	s_mov_b32 s69, s37
	s_waitcnt lgkmcnt(0)
	v_add_f32_e32 v50, v54, v55
	v_lshl_add_u64 v[48:49], v[48:49], 0, s[68:69]
	global_store_dword v[48:49], v50, off
.LBB0_917:
	s_or_b64 exec, exec, s[22:23]
	v_add_u32_e32 v48, 0x70, v146
	v_mul_f32_e32 v54, v37, v37
	s_waitcnt lgkmcnt(0)
	v_mul_f32_e32 v55, v39, v39
	v_ashrrev_i32_e32 v49, 31, v48
	v_fmac_f32_e32 v54, v36, v36
	v_fmac_f32_e32 v55, v38, v38
	v_lshlrev_b64 v[50:51], 12, v[48:49]
	v_add_f32_e32 v56, v54, v55
	v_mul_f32_e32 v54, v33, v33
	v_mul_f32_e32 v55, v35, v35
	v_lshl_add_u64 v[50:51], s[40:41], 0, v[50:51]
	v_fmac_f32_e32 v54, v32, v32
	v_fmac_f32_e32 v55, v34, v34
	v_lshl_add_u64 v[50:51], s[18:19], 1, v[50:51]
	v_mul_f32_e32 v52, v45, v45
	v_mul_f32_e32 v53, v47, v47
	v_add_f32_e32 v57, v54, v55
	v_mul_f32_e32 v54, v41, v41
	v_mul_f32_e32 v55, v43, v43
	v_lshl_add_u64 v[50:51], v[50:51], 0, s[36:37]
	v_fmac_f32_e32 v53, v46, v46
	v_fmac_f32_e32 v54, v40, v40
	v_fmac_f32_e32 v55, v42, v42
	v_fmac_f32_e32 v52, v44, v44
	v_add_f32_e32 v58, v54, v55
	v_lshl_add_u64 v[54:55], v[144:145], 1, v[50:51]
	v_cvt_pk_bf16_f32 v50, v44, v45
	v_add_f32_e32 v44, v52, v53
	v_add_f32_e32 v44, v44, v56
	v_add_f32_e32 v44, v44, v57
	v_add_f32_e32 v44, v44, v58
	v_mov_b32_e32 v45, v44
	s_nop 1
	v_permlane16_swap_b32 v44, v45
	v_cvt_pk_bf16_f32 v52, v36, v37
	v_cvt_pk_bf16_f32 v37, v34, v35
	v_cvt_pk_bf16_f32 v51, v46, v47
	v_cvt_pk_bf16_f32 v53, v38, v39
	s_waitcnt lgkmcnt(0)
	v_add_f32_e32 v34, v44, v45
	v_mov_b32_e32 v35, v34
	s_nop 1
	v_permlane32_swap_b32 v34, v35
	v_cvt_pk_bf16_f32 v36, v32, v33
	v_cvt_pk_bf16_f32 v39, v42, v43
	v_cvt_pk_bf16_f32 v38, v40, v41
	global_store_dwordx4 v[54:55], v[50:53], off
	global_store_dwordx4 v[54:55], v[36:39], off offset:64
	s_and_saveexec_b64 s[18:19], vcc
	s_cbranch_execz .LBB0_896
	s_lshl_b32 s22, s49, 2
	v_lshlrev_b64 v[32:33], 7, v[48:49]
	s_ashr_i32 s23, s22, 31
	v_lshl_add_u64 v[32:33], s[42:43], 0, v[32:33]
	v_lshl_add_u64 v[32:33], s[22:23], 2, v[32:33]
	s_lshl_b32 s22, s73, 2
	s_mov_b32 s23, s37
	s_waitcnt lgkmcnt(0)
	v_add_f32_e32 v34, v34, v35
	v_lshl_add_u64 v[32:33], v[32:33], 0, s[22:23]
	global_store_dword v[32:33], v34, off
	s_branch .LBB0_896
